# PV accumulator interleave: PV MFMAs alternate the two output accumulators (A1 A2 B1 A3 B2 A4 B3 B4), V^T fragment reads for the second accumulator issued in the first two gaps, counted lgkm waits
# speedup vs baseline: 1.0020x; 1.0011x over previous
.LBB0_1429:
	s_mov_b32 s4, s9
	s_mov_b32 s9, s22
	s_lshl_b32 s5, s10, 14
	s_add_i32 s5, s5, 0
	v_add_u32_e32 v54, s5, v167
	ds_read_b128 v[50:53], v54 offset:24576
	ds_read_b128 v[54:57], v54 offset:32768
	v_add_u32_e32 v148, s5, v168
	ds_read_b128 v[170:173], v148 offset:24576
	ds_read_b128 v[174:177], v148 offset:32768
	v_add_u32_e32 v148, s5, v166
	s_waitcnt lgkmcnt(3)
	v_mfma_f32_32x32x16_bf16 v[66:81], v[50:53], v[106:109], v[188:203]
	v_exp_f32_e32 v178, v42
	v_exp_f32_e32 v179, v43
	v_exp_f32_e32 v180, v44
	v_add_f32_e32 v143, v222, v227
	s_waitcnt lgkmcnt(2)
	v_mfma_f32_32x32x16_bf16 v[50:65], v[54:57], v[106:109], v[188:203]
	v_exp_f32_e32 v181, v45
	v_exp_f32_e32 v182, v46
	v_exp_f32_e32 v183, v47
	v_add_f32_e32 v145, v223, v230
	s_waitcnt lgkmcnt(1)
	v_mfma_f32_32x32x16_bf16 v[66:81], v[170:173], v[102:105], v[66:81]
	v_exp_f32_e32 v184, v48
	v_exp_f32_e32 v49, v49
	v_exp_f32_e32 v153, v35
	v_add_f32_e32 v143, v231, v143
	s_waitcnt lgkmcnt(0)
	v_mfma_f32_32x32x16_bf16 v[50:65], v[174:177], v[102:105], v[50:65]
	v_exp_f32_e32 v185, v34
	v_exp_f32_e32 v186, v36
	v_exp_f32_e32 v187, v37
	v_add_f32_e32 v145, v232, v145
	ds_read_b128 v[170:173], v148 offset:24576
	ds_read_b128 v[174:177], v148 offset:32768
	v_add_u32_e32 v148, s5, v162
	s_waitcnt lgkmcnt(1)
	v_mfma_f32_32x32x16_bf16 v[66:81], v[170:173], v[98:101], v[66:81]
	v_exp_f32_e32 v147, v38
	v_exp_f32_e32 v152, v39
	v_exp_f32_e32 v204, v40
	v_add_f32_e32 v143, v233, v143
	s_waitcnt lgkmcnt(0)
	v_mfma_f32_32x32x16_bf16 v[50:65], v[174:177], v[98:101], v[50:65]
	v_exp_f32_e32 v205, v41
	v_add_f32_e32 v145, v234, v145
	v_add_f32_e32 v143, v235, v143
	v_add_f32_e32 v145, v236, v145
	v_add_f32_e32 v143, v237, v143
	v_add_f32_e32 v145, v238, v145
	ds_read_b128 v[170:173], v148 offset:24576
	ds_read_b128 v[174:177], v148 offset:32768
	v_add_u32_e32 v148, s5, v161
	s_waitcnt lgkmcnt(1)
	v_mfma_f32_32x32x16_bf16 v[66:81], v[170:173], v[94:97], v[66:81]
	v_add_f32_e32 v143, v239, v143
	v_add_f32_e32 v145, v240, v145
	v_add_f32_e32 v143, v241, v143
	v_add_f32_e32 v145, v246, v145
	v_add_f32_e32 v143, v185, v143
	v_add_f32_e32 v145, v153, v145
	v_add_f32_e32 v143, v186, v143
	s_waitcnt lgkmcnt(0)
	v_mfma_f32_32x32x16_bf16 v[50:65], v[174:177], v[94:97], v[50:65]
	v_add_f32_e32 v145, v187, v145
	v_add_f32_e32 v143, v147, v143
	v_add_f32_e32 v145, v152, v145
	v_add_f32_e32 v143, v204, v143
	v_add_f32_e32 v145, v205, v145
	v_add_f32_e32 v143, v178, v143
	v_add_f32_e32 v145, v179, v145
	ds_read_b128 v[170:173], v148 offset:24576
	ds_read_b128 v[174:177], v148 offset:32768
	v_add_u32_e32 v148, s5, v160
	v_lshl_add_u32 v247, s4, 13, v158
	ds_read_b64_tr_b16 v[206:207], v247 offset:0
	ds_read_b64_tr_b16 v[208:209], v247 offset:0x400
	ds_read_b64_tr_b16 v[210:211], v247 offset:0x800
	ds_read_b64_tr_b16 v[212:213], v247 offset:0xc00
	ds_read_b64_tr_b16 v[214:215], v247 offset:0x1000
	ds_read_b64_tr_b16 v[216:217], v247 offset:0x1400
	ds_read_b64_tr_b16 v[218:219], v247 offset:0x1800
	ds_read_b64_tr_b16 v[220:221], v247 offset:0x1c00
	s_waitcnt lgkmcnt(9)
	v_mfma_f32_32x32x16_bf16 v[66:81], v[170:173], v[90:93], v[66:81]
	v_add_f32_e32 v143, v180, v143
	v_add_f32_e32 v145, v181, v145
	v_add_f32_e32 v143, v182, v143
	v_add_f32_e32 v145, v183, v145
	v_add_f32_e32 v143, v184, v143
	v_add_f32_e32 v145, v49, v145
	v_cvt_pk_bf16_f32 v34, v222, v223
	s_waitcnt lgkmcnt(8)
	v_mfma_f32_32x32x16_bf16 v[50:65], v[174:177], v[90:93], v[50:65]
	v_cvt_pk_bf16_f32 v35, v227, v230
	v_cvt_pk_bf16_f32 v36, v231, v232
	v_cvt_pk_bf16_f32 v37, v233, v234
	v_cvt_pk_bf16_f32 v38, v235, v236
	v_cvt_pk_bf16_f32 v39, v237, v238
	v_cvt_pk_bf16_f32 v40, v239, v240
	v_cvt_pk_bf16_f32 v41, v241, v246
	ds_read_b128 v[170:173], v148 offset:24576
	ds_read_b128 v[174:177], v148 offset:32768
	s_waitcnt lgkmcnt(1)
	v_mfma_f32_32x32x16_bf16 v[66:81], v[170:173], v[86:89], v[66:81]
	v_cvt_pk_bf16_f32 v42, v185, v153
	v_cvt_pk_bf16_f32 v43, v186, v187
	v_cvt_pk_bf16_f32 v44, v147, v152
	v_cvt_pk_bf16_f32 v45, v204, v205
	v_cvt_pk_bf16_f32 v46, v178, v179
	v_cvt_pk_bf16_f32 v47, v180, v181
	v_cvt_pk_bf16_f32 v48, v182, v183
	s_waitcnt lgkmcnt(0)
	v_mfma_f32_32x32x16_bf16 v[50:65], v[174:177], v[86:89], v[50:65]
	v_cvt_pk_bf16_f32 v49, v184, v49
	v_add_f32_e32 v170, v143, v145
	global_load_dwordx4 v[130:133], v146, s[84:85]
	global_load_dwordx4 v[126:129], v144, s[82:83]
	global_load_dwordx4 v[134:137], v142, s[82:83]
	s_add_u32 s82, s82, 0x3000
	s_addc_u32 s83, s83, 0
	s_add_u32 s84, s84, 0x2000
	s_addc_u32 s85, s85, 0
	s_waitcnt lgkmcnt(0)
	s_nop 0
	v_mfma_f32_32x32x16_bf16 v[2:17], v[34:37], v[206:209], v[2:17]
	ds_read_b64_tr_b16 v[172:173], v247 offset:0x200
	ds_read_b64_tr_b16 v[174:175], v247 offset:0x600
	ds_read_b64_tr_b16 v[176:177], v247 offset:0xa00
	ds_read_b64_tr_b16 v[178:179], v247 offset:0xe00
	v_max_f32_e32 v249, v67, v67
	v_max_f32_e32 v248, v66, v66
	v_max_f32_e32 v248, v248, v249
	v_max3_f32 v248, v248, v68, v69
	v_exp_f32_e32 v222, v66
	v_mfma_f32_32x32x16_bf16 v[2:17], v[38:41], v[210:213], v[2:17]
	ds_read_b64_tr_b16 v[180:181], v247 offset:0x1200
	ds_read_b64_tr_b16 v[182:183], v247 offset:0x1600
	ds_read_b64_tr_b16 v[184:185], v247 offset:0x1a00
	ds_read_b64_tr_b16 v[186:187], v247 offset:0x1e00
	v_max3_f32 v248, v248, v70, v71
	v_max3_f32 v248, v248, v72, v73
	v_max3_f32 v248, v248, v74, v75
	v_exp_f32_e32 v223, v67
	v_exp_f32_e32 v227, v68
	s_waitcnt lgkmcnt(6)
	v_mfma_f32_32x32x16_bf16 v[18:33], v[34:37], v[172:175], v[18:33]
	v_max3_f32 v248, v248, v76, v77
	v_max3_f32 v248, v248, v78, v79
	v_max3_f32 v248, v248, v80, v81
	v_exp_f32_e32 v230, v69
	v_exp_f32_e32 v231, v70
	v_mfma_f32_32x32x16_bf16 v[2:17], v[42:45], v[214:217], v[2:17]
	v_max3_f32 v248, v248, v50, v51
	v_max3_f32 v248, v248, v52, v53
	v_max3_f32 v248, v248, v54, v55
	v_exp_f32_e32 v232, v71
	v_exp_f32_e32 v233, v72
	s_waitcnt lgkmcnt(4)
	v_mfma_f32_32x32x16_bf16 v[18:33], v[38:41], v[176:179], v[18:33]
	s_lshl_b32 s11, s9, 13
	s_lshl_b32 s4, s9, 14
	s_add_i32 s6, s4, 0
	s_waitcnt vmcnt(3)
	v_add_u32_e32 v247, s11, v165
	ds_write_b128 v247, v[114:117]
	v_add_u32_e32 v247, s6, v163
	ds_write_b128 v247, v[118:121] offset:24576
	v_add_u32_e32 v247, s6, v164
	ds_write_b128 v247, v[122:125] offset:24576
	v_max3_f32 v248, v248, v56, v57
	v_max3_f32 v248, v248, v58, v59
	v_max3_f32 v248, v248, v60, v61
	v_exp_f32_e32 v234, v73
	v_exp_f32_e32 v235, v74
	v_mfma_f32_32x32x16_bf16 v[2:17], v[46:49], v[218:221], v[2:17]
	v_max3_f32 v248, v248, v62, v63
	v_max3_f32 v248, v248, v64, v65
	v_exp_f32_e32 v236, v75
	v_exp_f32_e32 v237, v76
	v_exp_f32_e32 v238, v77
	s_waitcnt lgkmcnt(5)
	v_mfma_f32_32x32x16_bf16 v[18:33], v[42:45], v[180:183], v[18:33]
	v_exp_f32_e32 v239, v78
	v_exp_f32_e32 v240, v79
	v_exp_f32_e32 v241, v80
	v_exp_f32_e32 v246, v81
	s_mov_b32 s4, 0x41380000
	v_cmp_ge_f32_e32 vcc, s4, v248
	s_waitcnt lgkmcnt(3)
	v_mfma_f32_32x32x16_bf16 v[18:33], v[46:49], v[184:187], v[18:33]
	s_cmp_eq_u64 vcc, exec
	s_cbranch_scc0 .LBB0_1448
	v_mov_b32_e32 v172, 1.0

.LBB0_1439:
	s_waitcnt lgkmcnt(0)
	s_nop 0
	v_mfma_f32_32x32x16_bf16 v[2:17], v[50:53], v[206:209], v[2:17]
	ds_read_b64_tr_b16 v[148:149], v247 offset:0x200
	ds_read_b64_tr_b16 v[150:151], v247 offset:0x600
	ds_read_b64_tr_b16 v[176:177], v247 offset:0xa00
	ds_read_b64_tr_b16 v[178:179], v247 offset:0xe00
	v_max_f32_e32 v249, v67, v67
	v_max_f32_e32 v248, v66, v66
	v_max_f32_e32 v248, v248, v249
	v_max3_f32 v248, v248, v68, v69
	v_exp_f32_e32 v222, v66
	v_mfma_f32_32x32x16_bf16 v[2:17], v[54:57], v[210:213], v[2:17]
	ds_read_b64_tr_b16 v[180:181], v247 offset:0x1200
	ds_read_b64_tr_b16 v[182:183], v247 offset:0x1600
	ds_read_b64_tr_b16 v[184:185], v247 offset:0x1a00
	ds_read_b64_tr_b16 v[186:187], v247 offset:0x1e00
	v_max3_f32 v248, v248, v70, v71
	v_max3_f32 v248, v248, v72, v73
	v_max3_f32 v248, v248, v74, v75
	v_exp_f32_e32 v223, v67
	v_exp_f32_e32 v227, v68
	s_waitcnt lgkmcnt(6)
	v_mfma_f32_32x32x16_bf16 v[18:33], v[50:53], v[148:151], v[18:33]
	v_max3_f32 v248, v248, v76, v77
	v_max3_f32 v248, v248, v78, v79
	v_max3_f32 v248, v248, v80, v81
	v_exp_f32_e32 v230, v69
	v_exp_f32_e32 v231, v70
	v_mfma_f32_32x32x16_bf16 v[2:17], v[58:61], v[214:217], v[2:17]
	v_max3_f32 v248, v248, v34, v35
	v_max3_f32 v248, v248, v36, v37
	v_max3_f32 v248, v248, v38, v39
	v_exp_f32_e32 v232, v71
	v_exp_f32_e32 v233, v72
	s_waitcnt lgkmcnt(4)
	v_mfma_f32_32x32x16_bf16 v[18:33], v[54:57], v[176:179], v[18:33]
	s_add_i32 s6, s9, 1
	s_cmp_lg_u32 s9, 2
	s_cselect_b32 s10, s6, 0
	s_lshl_b32 s20, s10, 13
	s_lshl_b32 s6, s10, 14
	s_add_i32 s21, s6, 0
	s_waitcnt vmcnt(3)
	v_add_u32_e32 v247, s20, v165
	ds_write_b128 v247, v[130:133]
	v_add_u32_e32 v247, s21, v163
	ds_write_b128 v247, v[126:129] offset:24576
	v_add_u32_e32 v247, s21, v164
	ds_write_b128 v247, v[134:137] offset:24576
	v_max3_f32 v248, v248, v40, v41
	v_max3_f32 v248, v248, v42, v43
	v_max3_f32 v248, v248, v44, v45
	v_exp_f32_e32 v234, v73
	v_exp_f32_e32 v235, v74
	v_mfma_f32_32x32x16_bf16 v[2:17], v[62:65], v[218:221], v[2:17]
	v_max3_f32 v248, v248, v46, v47
	v_max3_f32 v248, v248, v48, v49
	v_exp_f32_e32 v236, v75
	v_exp_f32_e32 v237, v76
	v_exp_f32_e32 v238, v77
	s_waitcnt lgkmcnt(5)
	v_mfma_f32_32x32x16_bf16 v[18:33], v[58:61], v[180:183], v[18:33]
	v_exp_f32_e32 v239, v78
	v_exp_f32_e32 v240, v79
	v_exp_f32_e32 v241, v80
	v_exp_f32_e32 v246, v81
	s_mov_b32 s6, 0x41380000
	v_cmp_ge_f32_e32 vcc, s6, v248
	s_waitcnt lgkmcnt(3)
	v_mfma_f32_32x32x16_bf16 v[18:33], v[62:65], v[184:187], v[18:33]
	s_cmp_eq_u64 vcc, exec
	v_mov_b32_e32 v148, 1.0
	s_cbranch_scc0 .LBB0_1449
